# attention loop step 2: K fragment ds_reads issued ahead of the LDS-DMA block, fp8 packs moved into the last two QK MFMA gaps
# baseline (speedup 1.0000x reference)
; #define SBAR() __builtin_amdgcn_sched_barrier(0)
; __device__ __forceinline__ void finishSM(f32x16& p0, f32x16& p1, float alpha, float& l_reg, v8i& pa) {
; #pragma unroll
;     for (int r = 0; r < 16; ++r) p1[r] = __builtin_amdgcn_exp2f(p1[r]);
;     float sa = p0[0] + p0[1], sb = p0[2] + p0[3], sc = p0[4] + p0[5], sd = p0[6] + p0[7];
;     sa += p0[8]; sb += p0[9]; sc += p0[10]; sd += p0[11]; sa += p0[12]; sb += p0[13]; sc += p0[14]; sd += p0[15];
; #pragma unroll
;     for (int r = 0; r < 16; r += 4) { sa += p1[r]; sb += p1[r + 1]; sc += p1[r + 2]; sd += p1[r + 3]; }
;     float ps = (sa + sb) + (sc + sd);
;     { auto rr = __builtin_amdgcn_permlane32_swap(__float_as_uint(ps), __float_as_uint(ps), false, false);
;       ps = __uint_as_float(rr[0]) + __uint_as_float(rr[1]); }
;     l_reg = l_reg * alpha + ps;
; #pragma unroll
;     for (int c = 0; c < 4; ++c) { pa[c] = (int)pk4_fp8(p0[4 * c], p0[4 * c + 1], p0[4 * c + 2], p0[4 * c + 3]);
;         pa[4 + c] = (int)pk4_fp8(p1[4 * c], p1[4 * c + 1], p1[4 * c + 2], p1[4 * c + 3]); }
; }
; __device__ __forceinline__ void qkt(f32x16& p0, f32x16& p1, const float m_reg, const char* Ks, const v8i* q8, int r32, int hi) {
;     { const float ini = PSH - m_reg;
; #pragma unroll
;       for (int r = 0; r < 16; ++r) { p0[r] = ini; p1[r] = ini; } }
; #pragma unroll
;     for (int ks = 0; ks < 3; ++ks) { const char* kp = Ks + r32 * KROWB + ks * 64 + hi * 32;
;         const v8i a0 = __builtin_shufflevector(*reinterpret_cast<const v4i*>(kp), *reinterpret_cast<const v4i*>(kp + 16), 0, 1, 2, 3, 4, 5, 6, 7);
;         const v8i a1 = __builtin_shufflevector(*reinterpret_cast<const v4i*>(kp + 32 * KROWB), *reinterpret_cast<const v4i*>(kp + 32 * KROWB + 16), 0, 1, 2, 3, 4, 5, 6, 7);
;         p0 = __builtin_amdgcn_mfma_scale_f32_32x32x64_f8f6f4(a0, q8[ks], p0, 0, 0, 0, QK_E, 0, QC_E);
; __device__ __forceinline__ void attn_unit(const bf16_t* Qb, const unsigned char* Kh, const unsigned char* Vh, bf16_t* Ob, int seq, int cbase, int lbase, int t0, const f32x2* atab, char* lds, const int wave_s) {
;     ...
;         { const int bn = 3 - bprev - bj; DMA_TILE(j + 1, bn);
;           SBAR(); qkt(pB0, pB1, m_reg, KBUF(bj), qr, r32, hi);
;           finishSM(pA0, pA1, alA, l_reg, pa); SBAR();
;           pv_d0(o, VBASE(bprev), pa, r32, hi); partialSM(pB0, pB1, m_reg, alB, false);
;           RESC(alB); WAITBAR(); bprev = bj; bj = bn; }
.LBB0_549:
	s_mul_i32 s0, s11, 0x5c00
	s_add_i32 s12, s0, 0
	v_add3_u32 v164, s12, v177, v161
	ds_read_b128 v[96:99], v164
	ds_read_b128 v[100:103], v164 offset:16
	ds_read_b128 v[136:139], v164 offset:6656
	ds_read_b128 v[140:143], v164 offset:6672
	s_add_i32 s0, s9, s11
	s_mov_b32 s10, s9
	s_sub_i32 s9, 3, s0
	s_sub_i32 s0, s8, 64
	s_cmp_lt_u32 s13, 3
	s_cselect_b32 s0, s7, s0
	s_mul_hi_i32 s1, s0, 0x300
	s_mulk_i32 s0, 0x300
	s_add_u32 s0, s55, s0
	s_mul_i32 s5, s9, 0x5c00
	s_addc_u32 s1, s56, s1
	s_add_i32 s2, s77, s5
	v_lshl_add_u64 v[166:167], s[0:1], 0, v[152:153]
	s_mov_b32 m0, s2
	s_and_b64 vcc, exec, s[46:47]
	global_load_lds_dwordx4 v[166:167], off
	s_cbranch_vccnz .LBB0_551
	v_lshl_add_u64 v[166:167], s[0:1], 0, v[156:157]
	s_add_i32 m0, s2, 0x2000
	s_nop 0
	global_load_lds_dwordx4 v[166:167], off
.LBB0_551:
	s_add_i32 m0, s2, 0x3400
	s_and_b64 vcc, exec, s[48:49]
	global_load_lds_dwordx4 v[158:159], off
	s_cbranch_vccnz .LBB0_553
	s_mov_b64 s[0:1], 0x2000
	v_lshl_add_u64 v[166:167], v[158:159], 0, s[0:1]
	s_add_i32 m0, s2, 0x5400
	s_nop 0
	global_load_lds_dwordx4 v[166:167], off
.LBB0_553:
	v_sub_f32_e32 v80, 0x40400000, v180
	v_mov_b32_e32 v81, v80
	v_mov_b32_e32 v82, v80
	v_mov_b32_e32 v83, v80
	v_mov_b32_e32 v84, v80
	v_mov_b32_e32 v85, v80
	v_mov_b32_e32 v86, v80
	v_mov_b32_e32 v87, v80
	v_mov_b32_e32 v88, v80
	v_mov_b32_e32 v89, v80
	v_mov_b32_e32 v90, v80
	v_mov_b32_e32 v91, v80
	v_mov_b32_e32 v92, v80
	v_mov_b32_e32 v93, v80
	v_mov_b32_e32 v94, v80
	v_mov_b32_e32 v95, v80
	v_exp_f32_e32 v228, v64
	v_exp_f32_e32 v230, v65
	s_waitcnt lgkmcnt(0)
	v_mfma_scale_f32_32x32x64_f8f6f4 v[96:111], v[96:103], v[120:127], v[80:95], v201, v200 op_sel_hi:[0,0,0]
	v_exp_f32_e32 v222, v66
	v_exp_f32_e32 v223, v67
	v_exp_f32_e32 v229, v68
	v_exp_f32_e32 v231, v69
	v_exp_f32_e32 v226, v70
	v_exp_f32_e32 v227, v71
	v_add_f32_e32 v64, v215, v216
	v_add_f32_e32 v65, v190, v192
	v_add_f32_e32 v66, v213, v214
	v_add_f32_e32 v67, v195, v212
	v_exp_f32_e32 v224, v72
	v_exp_f32_e32 v225, v73
	v_exp_f32_e32 v184, v74
	v_exp_f32_e32 v217, v75
	v_add_f32_e32 v64, v194, v64
	v_mfma_scale_f32_32x32x64_f8f6f4 v[80:95], v[136:143], v[120:127], v[80:95], v201, v200 op_sel_hi:[0,0,0]
	ds_read_b128 v[136:139], v164 offset:64
	ds_read_b128 v[140:143], v164 offset:80
	ds_read_b128 v[144:147], v164 offset:6720
	ds_read_b128 v[148:151], v164 offset:6736
	v_add_f32_e32 v65, v211, v65
	v_add_f32_e32 v66, v186, v66
	v_add_f32_e32 v67, v187, v67
	v_exp_f32_e32 v220, v76
	v_exp_f32_e32 v221, v77
	v_exp_f32_e32 v218, v78
	v_exp_f32_e32 v219, v79
	v_add_f32_e32 v64, v191, v64
	v_add_f32_e32 v65, v193, v65
	v_add_f32_e32 v66, v188, v66
	v_add_f32_e32 v67, v189, v67
	v_add_f32_e32 v64, v228, v64
	v_add_f32_e32 v65, v230, v65
	v_add_f32_e32 v66, v222, v66
	s_waitcnt lgkmcnt(0)
	v_mfma_scale_f32_32x32x64_f8f6f4 v[96:111], v[136:143], v[128:135], v[96:111], v201, v200 op_sel_hi:[0,0,0]
	v_add_f32_e32 v67, v223, v67
	v_add_f32_e32 v64, v229, v64
	v_add_f32_e32 v65, v231, v65
	v_add_f32_e32 v66, v226, v66
	v_add_f32_e32 v67, v227, v67
	v_add_f32_e32 v64, v224, v64
	v_add_f32_e32 v65, v225, v65
	v_add_f32_e32 v66, v184, v66
	v_add_f32_e32 v67, v217, v67
	v_add_f32_e32 v64, v220, v64
	v_add_f32_e32 v65, v221, v65
	v_add_f32_e32 v66, v218, v66
	v_add_f32_e32 v67, v219, v67
	v_add_f32_e32 v64, v65, v64
	v_add_f32_e32 v65, v66, v67
	v_mfma_scale_f32_32x32x64_f8f6f4 v[80:95], v[144:151], v[128:135], v[80:95], v201, v200 op_sel_hi:[0,0,0]
	ds_read_b128 v[136:139], v164 offset:128
	ds_read_b128 v[140:143], v164 offset:144
	ds_read_b128 v[144:147], v164 offset:6784
	ds_read_b128 v[148:151], v164 offset:6800
	v_add_f32_e32 v182, v65, v64
	v_mov_b32_e32 v183, v182
	v_cvt_pk_fp8_f32 v232, v215, v216
	v_cvt_pk_fp8_f32 v236, v228, v230
	v_cvt_pk_fp8_f32 v233, v213, v214
	v_cvt_pk_fp8_f32 v237, v229, v231
	v_cvt_pk_fp8_f32 v234, v194, v211
	v_cvt_pk_fp8_f32 v238, v224, v225
	v_cvt_pk_fp8_f32 v235, v191, v193
	v_cvt_pk_fp8_f32 v239, v220, v221
	v_permlane32_swap_b32_e32 v182, v183
	s_waitcnt lgkmcnt(0)
	v_mfma_scale_f32_32x32x64_f8f6f4 v[96:111], v[136:143], v[112:119], v[96:111], v201, v200 op_sel_hi:[0,0,0]
	v_cvt_pk_fp8_f32 v232, v190, v192 op_sel:[0,0,1]
	v_cvt_pk_fp8_f32 v236, v222, v223 op_sel:[0,0,1]
	v_cvt_pk_fp8_f32 v233, v195, v212 op_sel:[0,0,1]
	v_cvt_pk_fp8_f32 v237, v226, v227 op_sel:[0,0,1]
	v_cvt_pk_fp8_f32 v234, v186, v187 op_sel:[0,0,1]
	v_cvt_pk_fp8_f32 v238, v184, v217 op_sel:[0,0,1]
	v_cvt_pk_fp8_f32 v235, v188, v189 op_sel:[0,0,1]
	v_cvt_pk_fp8_f32 v239, v218, v219 op_sel:[0,0,1]
	v_mfma_scale_f32_32x32x64_f8f6f4 v[80:95], v[144:151], v[112:119], v[80:95], v201, v200 op_sel_hi:[0,0,0]
	s_mul_i32 s15, s10, 0x5c00
	s_add_i32 s11, s15, 0
	v_add_u32_e32 v64, s11, v161
	v_add_u32_e32 v176, v64, v179
	ds_read_b128 v[144:147], v176 offset:13312
	ds_read_b128 v[148:151], v176 offset:13328
	ds_read_b128 v[136:139], v176 offset:15872
	ds_read_b128 v[140:143], v176 offset:15888
	ds_read_b128 v[72:75], v176 offset:18432
	ds_read_b128 v[76:79], v176 offset:18448
	ds_read_b128 v[64:67], v176 offset:20992
	ds_read_b128 v[68:71], v176 offset:21008
	v_max_f32_e32 v164, v97, v97
	v_max_f32_e32 v165, v96, v96
	v_max_f32_e32 v164, v165, v164
	v_max3_f32 v165, v99, v100, v101
	v_max3_f32 v164, v164, v98, v108
	v_max3_f32 v165, v165, v110, v111
	v_max3_f32 v166, v102, v103, v104
	v_max3_f32 v167, v105, v106, v107
	s_waitcnt lgkmcnt(0)
	v_mfma_scale_f32_32x32x64_f8f6f4 v[0:15], v[232:239], v[144:151], v[0:15], v201, v201 op_sel_hi:[0,0,0]
	v_max3_f32 v164, v164, v109, v84
	v_max3_f32 v165, v165, v86, v87
	v_max3_f32 v166, v166, v80, v81
	v_max3_f32 v167, v167, v82, v83
	v_max3_f32 v164, v164, v85, v92
	v_max3_f32 v165, v165, v94, v95
	v_max3_f32 v166, v166, v88, v89
	v_max3_f32 v167, v167, v90, v91
	v_mfma_scale_f32_32x32x64_f8f6f4 v[48:63], v[232:239], v[136:143], v[48:63], v201, v201 op_sel_hi:[0,0,0]
	v_max3_f32 v164, v164, v93, v165
	v_max3_f32 v164, v164, v166, v167
	v_mov_b32_e32 v165, v164
	s_nop 1
	v_permlane32_swap_b32_e32 v164, v165
	v_max_f32_e32 v165, v165, v165
	v_max_f32_e32 v164, v164, v164
	v_max_f32_e32 v164, v164, v165
	v_add_f32_e32 v165, 0xc0400000, v164
	s_mov_b32 s0, 0x40b8aa3b
	v_cmp_ge_f32_e32 vcc, s0, v165
	s_cmp_eq_u64 vcc, exec
	v_mov_b32_e32 v185, 1.0
	s_cbranch_scc0 .LBB0_570

; __device__ __forceinline__ void finishSM(f32x16& p0, f32x16& p1, float alpha, float& l_reg, v8i& pa) {
; #pragma unroll
;     for (int r = 0; r < 16; ++r) p1[r] = __builtin_amdgcn_exp2f(p1[r]);
;     float sa = p0[0] + p0[1], sb = p0[2] + p0[3], sc = p0[4] + p0[5], sd = p0[6] + p0[7];
;     sa += p0[8]; sb += p0[9]; sc += p0[10]; sd += p0[11]; sa += p0[12]; sb += p0[13]; sc += p0[14]; sd += p0[15];
; #pragma unroll
;     for (int r = 0; r < 16; r += 4) { sa += p1[r]; sb += p1[r + 1]; sc += p1[r + 2]; sd += p1[r + 3]; }
;     float ps = (sa + sb) + (sc + sd);
;     { auto rr = __builtin_amdgcn_permlane32_swap(__float_as_uint(ps), __float_as_uint(ps), false, false);
;       ps = __uint_as_float(rr[0]) + __uint_as_float(rr[1]); }
;     l_reg = l_reg * alpha + ps;
; #pragma unroll
;     for (int c = 0; c < 4; ++c) { pa[c] = (int)pk4_fp8(p0[4 * c], p0[4 * c + 1], p0[4 * c + 2], p0[4 * c + 3]);
;         pa[4 + c] = (int)pk4_fp8(p1[4 * c], p1[4 * c + 1], p1[4 * c + 2], p1[4 * c + 3]); }
; }
; __device__ __forceinline__ void qkt(f32x16& p0, f32x16& p1, const float m_reg, const char* Ks, const v8i* q8, int r32, int hi) {
;     { const float ini = PSH - m_reg;
; #pragma unroll
;       for (int r = 0; r < 16; ++r) { p0[r] = ini; p1[r] = ini; } }
; #pragma unroll
;     for (int ks = 0; ks < 3; ++ks) { const char* kp = Ks + r32 * KROWB + ks * 64 + hi * 32;
;         const v8i a0 = __builtin_shufflevector(*reinterpret_cast<const v4i*>(kp), *reinterpret_cast<const v4i*>(kp + 16), 0, 1, 2, 3, 4, 5, 6, 7);
;         const v8i a1 = __builtin_shufflevector(*reinterpret_cast<const v4i*>(kp + 32 * KROWB), *reinterpret_cast<const v4i*>(kp + 32 * KROWB + 16), 0, 1, 2, 3, 4, 5, 6, 7);
;         p0 = __builtin_amdgcn_mfma_scale_f32_32x32x64_f8f6f4(a0, q8[ks], p0, 0, 0, 0, QK_E, 0, QC_E);
; __device__ __forceinline__ void attn_unit(const bf16_t* Qb, const unsigned char* Kh, const unsigned char* Vh, bf16_t* Ob, int seq, int cbase, int lbase, int t0, const f32x2* atab, char* lds, const int wave_s) {
;     ...
;         { const int bn = 3 - bprev - bj; if (j + 2 < NT) DMA_TILE(j + 2, bn);
;           SBAR(); qkt(pA0, pA1, m_reg, KBUF(bj), qr, r32, hi);
;           finishSM(pB0, pB1, alB, l_reg, pa); SBAR();
;           pv_d0(o, VBASE(bprev), pa, r32, hi); partialSM(pA0, pA1, m_reg, alA, false);
;           RESC(alA); WAITBAR(); bprev = bj; bj = bn; }
.LBB0_558:
	s_waitcnt vmcnt(0)
	s_add_i32 s14, s13, 2
	s_cmp_ge_i32 s14, s6
	s_waitcnt vmcnt(0)
	s_barrier
	v_add_u32_e32 v164, s5, v178
	ds_read_b128 v[96:99], v164
	ds_read_b128 v[100:103], v164 offset:16
	ds_read_b128 v[136:139], v164 offset:6656
	ds_read_b128 v[140:143], v164 offset:6672
	s_cbranch_scc1 .LBB0_563
	s_add_i32 s0, s7, 64
	s_cmp_lt_u32 s13, 2
	s_cselect_b32 s0, s0, s8
	s_mul_hi_i32 s1, s0, 0x300
	s_mulk_i32 s0, 0x300
	s_add_u32 s0, s55, s0
	s_addc_u32 s1, s56, s1
	s_add_i32 s13, s77, s15
	v_lshl_add_u64 v[166:167], s[0:1], 0, v[152:153]
	s_mov_b32 m0, s13
	s_and_b64 vcc, exec, s[46:47]
	global_load_lds_dwordx4 v[166:167], off
	s_cbranch_vccnz .LBB0_561
	v_lshl_add_u64 v[166:167], s[0:1], 0, v[156:157]
	s_add_i32 m0, s13, 0x2000
	s_nop 0
	global_load_lds_dwordx4 v[166:167], off
.LBB0_561:
	s_mov_b64 s[0:1], 0x2800
	v_lshl_add_u64 v[166:167], v[158:159], 0, s[0:1]
	s_add_i32 m0, s13, 0x3400
	s_and_b64 vcc, exec, s[48:49]
	global_load_lds_dwordx4 v[166:167], off
	s_cbranch_vccnz .LBB0_563
	s_mov_b64 s[0:1], 0x4800
	v_lshl_add_u64 v[166:167], v[158:159], 0, s[0:1]
	s_add_i32 m0, s13, 0x5400
	s_nop 0
	global_load_lds_dwordx4 v[166:167], off
.LBB0_563:
	v_sub_f32_e32 v64, 0x40400000, v180
	v_mov_b32_e32 v65, v64
	v_mov_b32_e32 v66, v64
	v_mov_b32_e32 v67, v64
	v_mov_b32_e32 v68, v64
	v_mov_b32_e32 v69, v64
	v_mov_b32_e32 v70, v64
	v_mov_b32_e32 v71, v64
	v_mov_b32_e32 v72, v64
	v_mov_b32_e32 v73, v64
	v_mov_b32_e32 v74, v64
	v_mov_b32_e32 v75, v64
	v_mov_b32_e32 v76, v64
	v_mov_b32_e32 v77, v64
	v_mov_b32_e32 v78, v64
	v_mov_b32_e32 v79, v64
	v_exp_f32_e32 v231, v80
	v_exp_f32_e32 v233, v81
	s_waitcnt lgkmcnt(0)
	v_mfma_scale_f32_32x32x64_f8f6f4 v[96:111], v[96:103], v[120:127], v[64:79], v201, v200 op_sel_hi:[0,0,0]
	v_exp_f32_e32 v225, v82
	v_exp_f32_e32 v226, v83
	v_exp_f32_e32 v232, v84
	v_exp_f32_e32 v234, v85
	v_exp_f32_e32 v229, v86
	v_exp_f32_e32 v230, v87
	v_add_f32_e32 v80, v216, v215
	v_add_f32_e32 v81, v194, v192
	v_add_f32_e32 v82, v214, v213
	v_add_f32_e32 v83, v212, v211
	v_exp_f32_e32 v227, v88
	v_exp_f32_e32 v228, v89
	v_exp_f32_e32 v219, v90
	v_exp_f32_e32 v220, v91
	v_add_f32_e32 v80, v193, v80
	v_mfma_scale_f32_32x32x64_f8f6f4 v[64:79], v[136:143], v[120:127], v[64:79], v201, v200 op_sel_hi:[0,0,0]
	ds_read_b128 v[136:139], v164 offset:64
	ds_read_b128 v[140:143], v164 offset:80
	ds_read_b128 v[144:147], v164 offset:6720
	ds_read_b128 v[148:151], v164 offset:6736
	v_add_f32_e32 v81, v195, v81
	v_add_f32_e32 v82, v186, v82
	v_add_f32_e32 v83, v187, v83
	v_exp_f32_e32 v223, v92
	v_exp_f32_e32 v224, v93
	v_exp_f32_e32 v221, v94
	v_exp_f32_e32 v222, v95
	v_add_f32_e32 v80, v190, v80
	v_add_f32_e32 v81, v191, v81
	v_add_f32_e32 v82, v188, v82
	v_add_f32_e32 v83, v189, v83
	v_add_f32_e32 v80, v80, v231
	v_add_f32_e32 v81, v81, v233
	v_add_f32_e32 v82, v82, v225
	s_waitcnt lgkmcnt(0)
	v_mfma_scale_f32_32x32x64_f8f6f4 v[96:111], v[136:143], v[128:135], v[96:111], v201, v200 op_sel_hi:[0,0,0]
	v_add_f32_e32 v83, v83, v226
	v_add_f32_e32 v80, v232, v80
	v_add_f32_e32 v81, v234, v81
	v_add_f32_e32 v82, v229, v82
	v_add_f32_e32 v83, v230, v83
	v_add_f32_e32 v80, v227, v80
	v_add_f32_e32 v81, v228, v81
	v_add_f32_e32 v82, v219, v82
	v_add_f32_e32 v83, v220, v83
	v_add_f32_e32 v80, v223, v80
	v_add_f32_e32 v81, v224, v81
	v_add_f32_e32 v82, v221, v82
	v_add_f32_e32 v83, v222, v83
	v_add_f32_e32 v80, v81, v80
	v_add_f32_e32 v81, v82, v83
	v_mfma_scale_f32_32x32x64_f8f6f4 v[64:79], v[144:151], v[128:135], v[64:79], v201, v200 op_sel_hi:[0,0,0]
	ds_read_b128 v[136:139], v164 offset:128
	ds_read_b128 v[140:143], v164 offset:144
	ds_read_b128 v[144:147], v164 offset:6784
	ds_read_b128 v[148:151], v164 offset:6800
	v_add_f32_e32 v217, v81, v80
	v_mov_b32_e32 v218, v217
	v_cvt_pk_fp8_f32 v236, v215, v216
	v_cvt_pk_fp8_f32 v240, v231, v233
	v_cvt_pk_fp8_f32 v237, v213, v214
	v_cvt_pk_fp8_f32 v241, v232, v234
	v_cvt_pk_fp8_f32 v238, v193, v195
	v_cvt_pk_fp8_f32 v242, v227, v228
	v_cvt_pk_fp8_f32 v239, v190, v191
	v_cvt_pk_fp8_f32 v243, v223, v224
	v_permlane32_swap_b32_e32 v217, v218
	s_waitcnt lgkmcnt(0)
	v_mfma_scale_f32_32x32x64_f8f6f4 v[96:111], v[136:143], v[112:119], v[96:111], v201, v200 op_sel_hi:[0,0,0]
	v_cvt_pk_fp8_f32 v236, v192, v194 op_sel:[0,0,1]
	v_cvt_pk_fp8_f32 v240, v225, v226 op_sel:[0,0,1]
	v_cvt_pk_fp8_f32 v237, v211, v212 op_sel:[0,0,1]
	v_cvt_pk_fp8_f32 v241, v229, v230 op_sel:[0,0,1]
	v_cvt_pk_fp8_f32 v238, v186, v187 op_sel:[0,0,1]
	v_cvt_pk_fp8_f32 v242, v219, v220 op_sel:[0,0,1]
	v_cvt_pk_fp8_f32 v239, v188, v189 op_sel:[0,0,1]
	v_cvt_pk_fp8_f32 v243, v221, v222 op_sel:[0,0,1]
	v_mfma_scale_f32_32x32x64_f8f6f4 v[64:79], v[144:151], v[112:119], v[64:79], v201, v200 op_sel_hi:[0,0,0]
	v_add3_u32 v84, s12, v161, v179
	ds_read_b128 v[144:147], v84 offset:13312
	ds_read_b128 v[148:151], v84 offset:13328
	ds_read_b128 v[136:139], v84 offset:15872
	ds_read_b128 v[140:143], v84 offset:15888
	ds_read_b128 v[88:91], v84 offset:18432
	ds_read_b128 v[92:95], v84 offset:18448
	ds_read_b128 v[80:83], v84 offset:20992
	ds_read_b128 v[84:87], v84 offset:21008
	s_nop 1
	v_max_f32_e32 v164, v97, v97
	v_max_f32_e32 v165, v96, v96
	v_max_f32_e32 v164, v165, v164
	v_max3_f32 v165, v99, v100, v101
	v_max3_f32 v164, v164, v98, v108
	v_max3_f32 v165, v165, v110, v111
	v_max3_f32 v166, v102, v103, v104
	v_max3_f32 v167, v105, v106, v107
	s_waitcnt lgkmcnt(0)
	v_mfma_scale_f32_32x32x64_f8f6f4 v[0:15], v[236:243], v[144:151], v[0:15], v201, v201 op_sel_hi:[0,0,0]
	v_max3_f32 v164, v164, v109, v68
	v_max3_f32 v165, v165, v70, v71
	v_max3_f32 v166, v166, v64, v65
	v_max3_f32 v167, v167, v66, v67
	v_max3_f32 v164, v164, v69, v76
	v_max3_f32 v165, v165, v78, v79
	v_max3_f32 v166, v166, v72, v73
	v_max3_f32 v167, v167, v74, v75
	v_mfma_scale_f32_32x32x64_f8f6f4 v[48:63], v[236:243], v[136:143], v[48:63], v201, v201 op_sel_hi:[0,0,0]
	v_max3_f32 v164, v164, v77, v165
	v_max3_f32 v164, v164, v166, v167
	v_mov_b32_e32 v165, v164
	s_nop 1
	v_permlane32_swap_b32_e32 v164, v165
	v_max_f32_e32 v165, v165, v165
	v_max_f32_e32 v164, v164, v164
	v_max_f32_e32 v164, v164, v165
	v_add_f32_e32 v165, 0xc0400000, v164
	s_mov_b32 s0, 0x40b8aa3b
	v_cmp_ge_f32_e32 vcc, s0, v165
	s_cmp_eq_u64 vcc, exec
	v_mov_b32_e32 v184, 1.0
	s_cbranch_scc0 .LBB0_571
